# P6 epilogue: the eight per-column coefficient loads issued together (one wait) instead of four dependent round trips behind vmcnt(0)
# baseline (speedup 1.0000x reference)
.LBB0_616:
	s_lshr_b32 s21, s26, 5
	s_mul_i32 s28, s21, 0x3000
	s_ashr_i32 s29, s28, 31
	v_lshl_or_b32 v242, s27, 8, v233
	s_lshl_b64 s[28:29], s[28:29], 2
	s_add_u32 s28, s49, s28
	v_ashrrev_i32_e32 v243, 31, v242
	s_addc_u32 s29, s54, s29
	v_lshlrev_b64 v[138:139], 2, v[242:243]
	v_lshl_add_u64 v[140:141], s[28:29], 0, v[138:139]
	v_lshl_add_u64 v[142:143], s[12:13], 0, v[138:139]
	global_load_dwordx4 v[126:129], v[140:141], off
	global_load_dwordx4 v[130:133], v[142:143], off
	global_load_dwordx4 v[146:149], v[140:141], off offset:64
	global_load_dwordx4 v[150:153], v[142:143], off offset:64
	global_load_dwordx4 v[154:157], v[140:141], off offset:512
	global_load_dwordx4 v[158:161], v[142:143], off offset:512
	global_load_dwordx4 v[162:165], v[140:141], off offset:576
	global_load_dwordx4 v[166:169], v[142:143], off offset:576
	v_lshl_add_u32 v224, s26, 8, v1
	v_ashrrev_i32_e32 v225, 31, v224
	v_lshl_add_u64 v[226:227], v[224:225], 2, s[10:11]
	global_load_dword v240, v[226:227], off
	v_lshl_add_u64 v[222:223], s[52:53], 0, v[138:139]
	v_or_b32_e32 v238, 16, v224
	v_ashrrev_i32_e32 v239, 31, v238
	v_or_b32_e32 v234, 32, v224
	v_ashrrev_i32_e32 v235, 31, v234
	v_or_b32_e32 v230, 48, v224
	v_ashrrev_i32_e32 v231, 31, v230
	v_cvt_f32_i32_e32 v135, v135
	v_cvt_f32_i32_e32 v134, v134
	v_cvt_f32_i32_e32 v137, v137
	v_cvt_f32_i32_e32 v136, v136
	v_cvt_f32_i32_e32 v123, v123
	v_cvt_f32_i32_e32 v122, v122
	v_cvt_f32_i32_e32 v125, v125
	v_cvt_f32_i32_e32 v124, v124
	v_lshlrev_b64 v[244:245], 12, v[224:225]
	v_cvt_f32_i32_e32 v119, v119
	v_cvt_f32_i32_e32 v118, v118
	v_cvt_f32_i32_e32 v121, v121
	v_cvt_f32_i32_e32 v120, v120
	v_cvt_f32_i32_e32 v115, v115
	v_cvt_f32_i32_e32 v114, v114
	v_cvt_f32_i32_e32 v117, v117
	v_cvt_f32_i32_e32 v116, v116
	v_cvt_f32_i32_e32 v111, v111
	v_cvt_f32_i32_e32 v110, v110
	v_cvt_f32_i32_e32 v113, v113
	v_cvt_f32_i32_e32 v112, v112
	v_cvt_f32_i32_e32 v107, v107
	v_cvt_f32_i32_e32 v106, v106
	v_cvt_f32_i32_e32 v109, v109
	v_cvt_f32_i32_e32 v108, v108
	v_cvt_f32_i32_e32 v103, v103
	v_cvt_f32_i32_e32 v102, v102
	v_cvt_f32_i32_e32 v105, v105
	v_cvt_f32_i32_e32 v104, v104
	v_cvt_f32_i32_e32 v99, v99
	v_cvt_f32_i32_e32 v98, v98
	v_cvt_f32_i32_e32 v101, v101
	v_cvt_f32_i32_e32 v100, v100
	v_cvt_f32_i32_e32 v95, v95
	v_cvt_f32_i32_e32 v94, v94
	v_cvt_f32_i32_e32 v97, v97
	v_cvt_f32_i32_e32 v96, v96
	v_cvt_f32_i32_e32 v91, v91
	v_cvt_f32_i32_e32 v90, v90
	v_cvt_f32_i32_e32 v93, v93
	v_cvt_f32_i32_e32 v92, v92
	v_cvt_f32_i32_e32 v87, v87
	v_cvt_f32_i32_e32 v86, v86
	v_cvt_f32_i32_e32 v89, v89
	v_cvt_f32_i32_e32 v88, v88
	v_cvt_f32_i32_e32 v83, v83
	v_cvt_f32_i32_e32 v82, v82
	v_cvt_f32_i32_e32 v85, v85
	v_cvt_f32_i32_e32 v84, v84
	v_cvt_f32_i32_e32 v79, v79
	v_cvt_f32_i32_e32 v78, v78
	v_cvt_f32_i32_e32 v81, v81
	v_cvt_f32_i32_e32 v80, v80
	v_cvt_f32_i32_e32 v75, v75
	v_cvt_f32_i32_e32 v74, v74
	v_cvt_f32_i32_e32 v77, v77
	v_cvt_f32_i32_e32 v76, v76
	v_cvt_f32_i32_e32 v71, v71
	v_cvt_f32_i32_e32 v70, v70
	v_cvt_f32_i32_e32 v73, v73
	v_cvt_f32_i32_e32 v72, v72
	v_cvt_f32_i32_e32 v67, v67
	v_cvt_f32_i32_e32 v66, v66
	v_cvt_f32_i32_e32 v69, v69
	v_cvt_f32_i32_e32 v68, v68
	v_cvt_f32_i32_e32 v63, v63
	v_cvt_f32_i32_e32 v62, v62
	v_cvt_f32_i32_e32 v65, v65
	v_cvt_f32_i32_e32 v64, v64
	s_waitcnt vmcnt(0)
	v_pk_mul_f32 v[128:129], v[128:129], v[132:133]
	v_pk_mul_f32 v[126:127], v[126:127], v[130:131]
	v_pk_mul_f32 v[218:219], v[128:129], s[18:19] op_sel_hi:[1,0]
	v_pk_mul_f32 v[220:221], v[126:127], s[18:19] op_sel_hi:[1,0]
	v_cvt_f32_i32_e32 v59, v59
	v_cvt_f32_i32_e32 v58, v58
	v_cvt_f32_i32_e32 v61, v61
	v_cvt_f32_i32_e32 v60, v60
	v_cvt_f32_i32_e32 v55, v55
	v_cvt_f32_i32_e32 v54, v54
	v_cvt_f32_i32_e32 v57, v57
	v_cvt_f32_i32_e32 v56, v56
	v_cvt_f32_i32_e32 v51, v51
	v_cvt_f32_i32_e32 v50, v50
	v_cvt_f32_i32_e32 v53, v53
	v_cvt_f32_i32_e32 v52, v52
	v_cvt_f32_i32_e32 v47, v47
	v_cvt_f32_i32_e32 v46, v46
	v_cvt_f32_i32_e32 v49, v49
	v_cvt_f32_i32_e32 v48, v48
	v_cvt_f32_i32_e32 v43, v43
	v_cvt_f32_i32_e32 v42, v42
	v_cvt_f32_i32_e32 v45, v45
	v_cvt_f32_i32_e32 v44, v44
	v_cvt_f32_i32_e32 v39, v39
	v_cvt_f32_i32_e32 v38, v38
	v_cvt_f32_i32_e32 v41, v41
	v_cvt_f32_i32_e32 v40, v40
	v_cvt_f32_i32_e32 v35, v35
	v_cvt_f32_i32_e32 v34, v34
	v_cvt_f32_i32_e32 v37, v37
	v_cvt_f32_i32_e32 v36, v36
	v_cvt_f32_i32_e32 v31, v31
	v_cvt_f32_i32_e32 v30, v30
	v_cvt_f32_i32_e32 v33, v33
	v_cvt_f32_i32_e32 v32, v32
	v_cvt_f32_i32_e32 v23, v23
	v_cvt_f32_i32_e32 v22, v22
	v_cvt_f32_i32_e32 v25, v25
	v_cvt_f32_i32_e32 v24, v24
	v_cvt_f32_i32_e32 v27, v27
	v_cvt_f32_i32_e32 v26, v26
	v_cvt_f32_i32_e32 v29, v29
	v_cvt_f32_i32_e32 v28, v28
	v_cvt_f32_i32_e32 v19, v19
	v_cvt_f32_i32_e32 v18, v18
	v_cvt_f32_i32_e32 v21, v21
	v_cvt_f32_i32_e32 v20, v20
	v_cvt_f32_i32_e32 v11, v11
	v_cvt_f32_i32_e32 v10, v10
	v_cvt_f32_i32_e32 v13, v13
	v_cvt_f32_i32_e32 v12, v12
	v_cvt_f32_i32_e32 v5, v5
	v_cvt_f32_i32_e32 v4, v4
	v_cvt_f32_i32_e32 v3, v3
	v_cvt_f32_i32_e32 v2, v2
	v_cvt_f32_i32_e32 v7, v7
	v_cvt_f32_i32_e32 v6, v6
	v_cvt_f32_i32_e32 v9, v9
	v_cvt_f32_i32_e32 v8, v8
	s_mov_b64 s[26:27], -1
	s_and_b64 vcc, exec, s[4:5]
	v_pk_mul_f32 v[148:149], v[148:149], v[152:153]
	v_pk_mul_f32 v[146:147], v[146:147], v[150:151]
	v_pk_mul_f32 v[214:215], v[148:149], s[18:19] op_sel_hi:[1,0]
	v_pk_mul_f32 v[216:217], v[146:147], s[18:19] op_sel_hi:[1,0]
	v_pk_mul_f32 v[156:157], v[156:157], v[160:161]
	v_pk_mul_f32 v[154:155], v[154:155], v[158:159]
	v_pk_mul_f32 v[210:211], v[156:157], s[18:19] op_sel_hi:[1,0]
	v_pk_mul_f32 v[212:213], v[154:155], s[18:19] op_sel_hi:[1,0]
	v_pk_mul_f32 v[162:163], v[162:163], v[166:167]
	v_pk_mul_f32 v[164:165], v[164:165], v[168:169]
	v_pk_mul_f32 v[206:207], v[164:165], s[18:19] op_sel_hi:[1,0]
	s_nop 0
	v_pk_mul_f32 v[208:209], v[162:163], s[18:19] op_sel_hi:[1,0]
	v_lshlrev_b64 v[126:127], 13, v[224:225]
	v_lshl_add_u64 v[126:127], v[222:223], 0, v[126:127]
	global_load_dwordx4 v[248:251], v[126:127], off
	global_load_dwordx4 v[186:189], v[126:127], off offset:64
	global_load_dwordx4 v[182:185], v[126:127], off offset:512
	global_load_dwordx4 v[178:181], v[126:127], off offset:576
	v_lshl_add_u64 v[126:127], v[238:239], 2, s[10:11]
	global_load_dword v236, v[126:127], off
	v_lshlrev_b64 v[126:127], 13, v[238:239]
	v_lshl_add_u64 v[126:127], v[222:223], 0, v[126:127]
	global_load_dwordx4 v[174:177], v[126:127], off
	global_load_dwordx4 v[170:173], v[126:127], off offset:64
	global_load_dwordx4 v[166:169], v[126:127], off offset:512
	global_load_dwordx4 v[162:165], v[126:127], off offset:576
	v_lshl_add_u64 v[126:127], v[234:235], 2, s[10:11]
	global_load_dword v232, v[126:127], off
	v_lshlrev_b64 v[126:127], 13, v[234:235]
	v_lshl_add_u64 v[126:127], v[222:223], 0, v[126:127]
	global_load_dwordx4 v[158:161], v[126:127], off
	global_load_dwordx4 v[154:157], v[126:127], off offset:64
	global_load_dwordx4 v[150:153], v[126:127], off offset:512
	global_load_dwordx4 v[146:149], v[126:127], off offset:576
	v_lshl_add_u64 v[126:127], v[230:231], 2, s[10:11]
	global_load_dword v228, v[126:127], off
	v_lshlrev_b64 v[126:127], 13, v[230:231]
	v_lshl_add_u64 v[126:127], v[222:223], 0, v[126:127]
	global_load_dwordx4 v[142:145], v[126:127], off
	global_load_dwordx4 v[138:141], v[126:127], off offset:64
	global_load_dwordx4 v[130:133], v[126:127], off offset:512
	s_nop 0
	global_load_dwordx4 v[126:129], v[126:127], off offset:576
	s_waitcnt vmcnt(19)
	v_pk_mul_f32 v[252:253], v[218:219], v[240:241] op_sel_hi:[1,0]
	v_pk_mul_f32 v[204:205], v[220:221], v[240:241] op_sel_hi:[1,0]
	s_waitcnt vmcnt(18)
	v_pk_fma_f32 v[136:137], v[252:253], v[136:137], v[250:251]
	v_pk_fma_f32 v[134:135], v[204:205], v[134:135], v[248:249]
	s_nop 0
	v_cvt_pk_bf16_f32 v204, v134, v135
	v_cvt_pk_bf16_f32 v205, v136, v137
	v_lshl_add_u64 v[136:137], s[8:9], 0, v[244:245]
	v_lshlrev_b64 v[134:135], 1, v[242:243]
	v_pk_mul_f32 v[244:245], v[214:215], v[240:241] op_sel_hi:[1,0]
	v_pk_mul_f32 v[242:243], v[216:217], v[240:241] op_sel_hi:[1,0]
	v_lshl_add_u64 v[136:137], v[136:137], 0, v[134:135]
	s_waitcnt vmcnt(17)
	v_pk_fma_f32 v[124:125], v[244:245], v[124:125], v[188:189]
	v_pk_fma_f32 v[122:123], v[242:243], v[122:123], v[186:187]
	global_store_dwordx2 v[136:137], v[204:205], off
	v_cvt_pk_bf16_f32 v122, v122, v123
	v_cvt_pk_bf16_f32 v123, v124, v125
	v_pk_mul_f32 v[124:125], v[212:213], v[240:241] op_sel_hi:[1,0]
	global_store_dwordx2 v[136:137], v[122:123], off offset:32
	v_pk_mul_f32 v[122:123], v[210:211], v[240:241] op_sel_hi:[1,0]
	s_waitcnt vmcnt(18)
	v_pk_fma_f32 v[118:119], v[124:125], v[118:119], v[182:183]
	v_pk_fma_f32 v[120:121], v[122:123], v[120:121], v[184:185]
	v_cvt_pk_bf16_f32 v118, v118, v119
	s_nop 0
	v_cvt_pk_bf16_f32 v119, v120, v121
	global_store_dwordx2 v[136:137], v[118:119], off offset:256
	v_pk_mul_f32 v[118:119], v[206:207], v[240:241] op_sel_hi:[1,0]
	v_pk_mul_f32 v[120:121], v[208:209], v[240:241] op_sel_hi:[1,0]
	s_waitcnt vmcnt(18)
	v_pk_fma_f32 v[116:117], v[118:119], v[116:117], v[180:181]
	v_pk_fma_f32 v[114:115], v[120:121], v[114:115], v[178:179]
	s_waitcnt vmcnt(17)
	v_pk_mul_f32 v[118:119], v[220:221], v[236:237] op_sel_hi:[1,0]
	v_cvt_pk_bf16_f32 v114, v114, v115
	v_cvt_pk_bf16_f32 v115, v116, v117
	v_pk_mul_f32 v[116:117], v[218:219], v[236:237] op_sel_hi:[1,0]
	global_store_dwordx2 v[136:137], v[114:115], off offset:288
	v_lshlrev_b64 v[114:115], 12, v[238:239]
	s_waitcnt vmcnt(17)
	v_pk_fma_f32 v[112:113], v[116:117], v[112:113], v[176:177]
	v_pk_fma_f32 v[110:111], v[118:119], v[110:111], v[174:175]
	v_add_u32_e32 v120, 0xa0, v224
	v_cvt_pk_bf16_f32 v110, v110, v111
	v_cvt_pk_bf16_f32 v111, v112, v113
	v_lshl_add_u64 v[112:113], s[8:9], 0, v[114:115]
	v_lshl_add_u64 v[112:113], v[112:113], 0, v[134:135]
	global_store_dwordx2 v[112:113], v[110:111], off
	v_pk_mul_f32 v[110:111], v[214:215], v[236:237] op_sel_hi:[1,0]
	v_pk_mul_f32 v[114:115], v[216:217], v[236:237] op_sel_hi:[1,0]
	s_waitcnt vmcnt(17)
	v_pk_fma_f32 v[108:109], v[110:111], v[108:109], v[172:173]
	v_pk_fma_f32 v[106:107], v[114:115], v[106:107], v[170:171]
	v_ashrrev_i32_e32 v121, 31, v120
	v_cvt_pk_bf16_f32 v106, v106, v107
	v_cvt_pk_bf16_f32 v107, v108, v109
	v_pk_mul_f32 v[108:109], v[212:213], v[236:237] op_sel_hi:[1,0]
	global_store_dwordx2 v[112:113], v[106:107], off offset:32
	v_pk_mul_f32 v[106:107], v[210:211], v[236:237] op_sel_hi:[1,0]
	s_waitcnt vmcnt(17)
	v_pk_fma_f32 v[102:103], v[108:109], v[102:103], v[166:167]
	v_pk_fma_f32 v[104:105], v[106:107], v[104:105], v[168:169]
	v_cvt_pk_bf16_f32 v102, v102, v103
	v_add_u32_e32 v116, 0xb0, v224
	v_cvt_pk_bf16_f32 v103, v104, v105
	global_store_dwordx2 v[112:113], v[102:103], off offset:256
	v_pk_mul_f32 v[102:103], v[206:207], v[236:237] op_sel_hi:[1,0]
	v_pk_mul_f32 v[104:105], v[208:209], v[236:237] op_sel_hi:[1,0]
	s_waitcnt vmcnt(17)
	v_pk_fma_f32 v[100:101], v[102:103], v[100:101], v[164:165]
	v_pk_fma_f32 v[98:99], v[104:105], v[98:99], v[162:163]
	s_waitcnt vmcnt(16)
	v_pk_mul_f32 v[102:103], v[220:221], v[232:233] op_sel_hi:[1,0]
	v_cvt_pk_bf16_f32 v98, v98, v99
	v_cvt_pk_bf16_f32 v99, v100, v101
	v_pk_mul_f32 v[100:101], v[218:219], v[232:233] op_sel_hi:[1,0]
	global_store_dwordx2 v[112:113], v[98:99], off offset:288
	v_lshlrev_b64 v[98:99], 12, v[234:235]
	s_waitcnt vmcnt(16)
	v_pk_fma_f32 v[96:97], v[100:101], v[96:97], v[160:161]
	v_pk_fma_f32 v[94:95], v[102:103], v[94:95], v[158:159]
	v_ashrrev_i32_e32 v117, 31, v116
	v_cvt_pk_bf16_f32 v94, v94, v95
	v_cvt_pk_bf16_f32 v95, v96, v97
	v_lshl_add_u64 v[96:97], s[8:9], 0, v[98:99]
	v_lshl_add_u64 v[96:97], v[96:97], 0, v[134:135]
	global_store_dwordx2 v[96:97], v[94:95], off
	v_pk_mul_f32 v[94:95], v[214:215], v[232:233] op_sel_hi:[1,0]
	v_pk_mul_f32 v[98:99], v[216:217], v[232:233] op_sel_hi:[1,0]
	s_waitcnt vmcnt(16)
	v_pk_fma_f32 v[92:93], v[94:95], v[92:93], v[156:157]
	v_pk_fma_f32 v[90:91], v[98:99], v[90:91], v[154:155]
	s_nop 0
	v_cvt_pk_bf16_f32 v90, v90, v91
	v_cvt_pk_bf16_f32 v91, v92, v93
	v_pk_mul_f32 v[92:93], v[212:213], v[232:233] op_sel_hi:[1,0]
	global_store_dwordx2 v[96:97], v[90:91], off offset:32
	v_pk_mul_f32 v[90:91], v[210:211], v[232:233] op_sel_hi:[1,0]
	s_waitcnt vmcnt(16)
	v_pk_fma_f32 v[86:87], v[92:93], v[86:87], v[150:151]
	v_pk_fma_f32 v[88:89], v[90:91], v[88:89], v[152:153]
	v_cvt_pk_bf16_f32 v86, v86, v87
	s_nop 0
	v_cvt_pk_bf16_f32 v87, v88, v89
	global_store_dwordx2 v[96:97], v[86:87], off offset:256
	v_pk_mul_f32 v[86:87], v[206:207], v[232:233] op_sel_hi:[1,0]
	v_pk_mul_f32 v[88:89], v[208:209], v[232:233] op_sel_hi:[1,0]
	s_waitcnt vmcnt(16)
	v_pk_fma_f32 v[84:85], v[86:87], v[84:85], v[148:149]
	v_pk_fma_f32 v[82:83], v[88:89], v[82:83], v[146:147]
	s_waitcnt vmcnt(15)
	v_pk_mul_f32 v[86:87], v[220:221], v[228:229] op_sel_hi:[1,0]
	v_cvt_pk_bf16_f32 v82, v82, v83
	v_cvt_pk_bf16_f32 v83, v84, v85
	v_pk_mul_f32 v[84:85], v[218:219], v[228:229] op_sel_hi:[1,0]
	global_store_dwordx2 v[96:97], v[82:83], off offset:288
	v_lshlrev_b64 v[82:83], 12, v[230:231]
	s_waitcnt vmcnt(15)
	v_pk_fma_f32 v[80:81], v[84:85], v[80:81], v[144:145]
	v_pk_fma_f32 v[78:79], v[86:87], v[78:79], v[142:143]
	v_add_u32_e32 v146, 0x90, v224
	v_cvt_pk_bf16_f32 v78, v78, v79
	v_cvt_pk_bf16_f32 v79, v80, v81
	v_lshl_add_u64 v[80:81], s[8:9], 0, v[82:83]
	v_lshl_add_u64 v[80:81], v[80:81], 0, v[134:135]
	v_pk_mul_f32 v[82:83], v[216:217], v[228:229] op_sel_hi:[1,0]
	global_store_dwordx2 v[80:81], v[78:79], off
	v_pk_mul_f32 v[78:79], v[214:215], v[228:229] op_sel_hi:[1,0]
	s_waitcnt vmcnt(15)
	v_pk_fma_f32 v[74:75], v[82:83], v[74:75], v[138:139]
	v_pk_fma_f32 v[76:77], v[78:79], v[76:77], v[140:141]
	v_cvt_pk_bf16_f32 v74, v74, v75
	v_ashrrev_i32_e32 v147, 31, v146
	v_cvt_pk_bf16_f32 v75, v76, v77
	global_store_dwordx2 v[80:81], v[74:75], off offset:32
	v_pk_mul_f32 v[74:75], v[210:211], v[228:229] op_sel_hi:[1,0]
	v_pk_mul_f32 v[76:77], v[212:213], v[228:229] op_sel_hi:[1,0]
	s_waitcnt vmcnt(15)
	v_pk_fma_f32 v[72:73], v[74:75], v[72:73], v[132:133]
	v_pk_fma_f32 v[70:71], v[76:77], v[70:71], v[130:131]
	v_add_u32_e32 v132, 0x80, v224
	v_cvt_pk_bf16_f32 v70, v70, v71
	v_cvt_pk_bf16_f32 v71, v72, v73
	v_pk_mul_f32 v[72:73], v[208:209], v[228:229] op_sel_hi:[1,0]
	global_store_dwordx2 v[80:81], v[70:71], off offset:256
	v_pk_mul_f32 v[70:71], v[206:207], v[228:229] op_sel_hi:[1,0]
	s_waitcnt vmcnt(15)
	v_pk_fma_f32 v[66:67], v[72:73], v[66:67], v[126:127]
	v_pk_fma_f32 v[68:69], v[70:71], v[68:69], v[128:129]
	v_cvt_pk_bf16_f32 v66, v66, v67
	v_ashrrev_i32_e32 v133, 31, v132
	v_cvt_pk_bf16_f32 v67, v68, v69
	global_store_dwordx2 v[80:81], v[66:67], off offset:288
	global_load_dword v144, v[226:227], off offset:512
	v_lshlrev_b64 v[66:67], 13, v[132:133]
	v_lshl_add_u64 v[66:67], v[222:223], 0, v[66:67]
	global_load_dwordx4 v[124:127], v[66:67], off
	global_load_dwordx4 v[128:131], v[66:67], off offset:64
	global_load_dwordx4 v[136:139], v[66:67], off offset:512
	global_load_dwordx4 v[140:143], v[66:67], off offset:576
	global_load_dword v122, v[226:227], off offset:576
	v_lshlrev_b64 v[66:67], 13, v[146:147]
	v_lshl_add_u64 v[66:67], v[222:223], 0, v[66:67]
	global_load_dwordx4 v[110:113], v[66:67], off
	global_load_dwordx4 v[106:109], v[66:67], off offset:64
	global_load_dwordx4 v[102:105], v[66:67], off offset:512
	global_load_dwordx4 v[98:101], v[66:67], off offset:576
	global_load_dword v118, v[226:227], off offset:640
	v_lshlrev_b64 v[66:67], 13, v[120:121]
	v_lshl_add_u64 v[66:67], v[222:223], 0, v[66:67]
	global_load_dwordx4 v[94:97], v[66:67], off
	global_load_dwordx4 v[90:93], v[66:67], off offset:64
	global_load_dwordx4 v[86:89], v[66:67], off offset:512
	global_load_dwordx4 v[82:85], v[66:67], off offset:576
	global_load_dword v114, v[226:227], off offset:704
	v_lshlrev_b64 v[66:67], 13, v[116:117]
	v_lshl_add_u64 v[66:67], v[222:223], 0, v[66:67]
	global_load_dwordx4 v[78:81], v[66:67], off
	global_load_dwordx4 v[74:77], v[66:67], off offset:64
	global_load_dwordx4 v[70:73], v[66:67], off offset:512
	s_nop 0
	global_load_dwordx4 v[66:69], v[66:67], off offset:576
	v_lshlrev_b64 v[132:133], 12, v[132:133]
	s_waitcnt vmcnt(19)
	v_pk_mul_f32 v[148:149], v[218:219], v[144:145] op_sel_hi:[1,0]
	v_pk_mul_f32 v[150:151], v[220:221], v[144:145] op_sel_hi:[1,0]
	s_waitcnt vmcnt(18)
	v_pk_fma_f32 v[64:65], v[148:149], v[64:65], v[126:127]
	v_pk_fma_f32 v[62:63], v[150:151], v[62:63], v[124:125]
	v_pk_mul_f32 v[124:125], v[216:217], v[144:145] op_sel_hi:[1,0]
	v_cvt_pk_bf16_f32 v62, v62, v63
	v_cvt_pk_bf16_f32 v63, v64, v65
	v_lshl_add_u64 v[64:65], s[8:9], 0, v[132:133]
	v_lshl_add_u64 v[64:65], v[64:65], 0, v[134:135]
	global_store_dwordx2 v[64:65], v[62:63], off
	v_pk_mul_f32 v[62:63], v[214:215], v[144:145] op_sel_hi:[1,0]
	s_waitcnt vmcnt(18)
	v_pk_fma_f32 v[58:59], v[124:125], v[58:59], v[128:129]
	v_pk_fma_f32 v[60:61], v[62:63], v[60:61], v[130:131]
	v_cvt_pk_bf16_f32 v58, v58, v59
	s_nop 0
	v_cvt_pk_bf16_f32 v59, v60, v61
	v_pk_mul_f32 v[60:61], v[212:213], v[144:145] op_sel_hi:[1,0]
	global_store_dwordx2 v[64:65], v[58:59], off offset:32
	v_pk_mul_f32 v[58:59], v[210:211], v[144:145] op_sel_hi:[1,0]
	s_waitcnt vmcnt(18)
	v_pk_fma_f32 v[54:55], v[60:61], v[54:55], v[136:137]
	v_pk_fma_f32 v[56:57], v[58:59], v[56:57], v[138:139]
	v_cvt_pk_bf16_f32 v54, v54, v55
	s_nop 0
	v_cvt_pk_bf16_f32 v55, v56, v57
	global_store_dwordx2 v[64:65], v[54:55], off offset:256
	v_pk_mul_f32 v[54:55], v[206:207], v[144:145] op_sel_hi:[1,0]
	v_pk_mul_f32 v[56:57], v[208:209], v[144:145] op_sel_hi:[1,0]
	s_waitcnt vmcnt(18)
	v_pk_fma_f32 v[52:53], v[54:55], v[52:53], v[142:143]
	v_pk_fma_f32 v[50:51], v[56:57], v[50:51], v[140:141]
	s_waitcnt vmcnt(17)
	v_pk_mul_f32 v[54:55], v[220:221], v[122:123] op_sel_hi:[1,0]
	v_cvt_pk_bf16_f32 v50, v50, v51
	v_cvt_pk_bf16_f32 v51, v52, v53
	v_pk_mul_f32 v[52:53], v[218:219], v[122:123] op_sel_hi:[1,0]
	global_store_dwordx2 v[64:65], v[50:51], off offset:288
	v_lshlrev_b64 v[50:51], 12, v[146:147]
	s_waitcnt vmcnt(17)
	v_pk_fma_f32 v[48:49], v[52:53], v[48:49], v[112:113]
	v_pk_fma_f32 v[46:47], v[54:55], v[46:47], v[110:111]
	s_nop 0
	v_cvt_pk_bf16_f32 v46, v46, v47
	v_cvt_pk_bf16_f32 v47, v48, v49
	v_lshl_add_u64 v[48:49], s[8:9], 0, v[50:51]
	v_lshl_add_u64 v[48:49], v[48:49], 0, v[134:135]
	global_store_dwordx2 v[48:49], v[46:47], off
	v_pk_mul_f32 v[46:47], v[214:215], v[122:123] op_sel_hi:[1,0]
	v_pk_mul_f32 v[50:51], v[216:217], v[122:123] op_sel_hi:[1,0]
	s_waitcnt vmcnt(17)
	v_pk_fma_f32 v[44:45], v[46:47], v[44:45], v[108:109]
	v_pk_fma_f32 v[42:43], v[50:51], v[42:43], v[106:107]
	s_nop 0
	v_cvt_pk_bf16_f32 v42, v42, v43
	v_cvt_pk_bf16_f32 v43, v44, v45
	v_pk_mul_f32 v[44:45], v[212:213], v[122:123] op_sel_hi:[1,0]
	global_store_dwordx2 v[48:49], v[42:43], off offset:32
	v_pk_mul_f32 v[42:43], v[210:211], v[122:123] op_sel_hi:[1,0]
	s_waitcnt vmcnt(17)
	v_pk_fma_f32 v[38:39], v[44:45], v[38:39], v[102:103]
	v_pk_fma_f32 v[40:41], v[42:43], v[40:41], v[104:105]
	v_cvt_pk_bf16_f32 v38, v38, v39
	s_nop 0
	v_cvt_pk_bf16_f32 v39, v40, v41
	global_store_dwordx2 v[48:49], v[38:39], off offset:256
	v_pk_mul_f32 v[38:39], v[206:207], v[122:123] op_sel_hi:[1,0]
	v_pk_mul_f32 v[40:41], v[208:209], v[122:123] op_sel_hi:[1,0]
	s_waitcnt vmcnt(17)
	v_pk_fma_f32 v[36:37], v[38:39], v[36:37], v[100:101]
	v_pk_fma_f32 v[34:35], v[40:41], v[34:35], v[98:99]
	s_waitcnt vmcnt(16)
	v_pk_mul_f32 v[38:39], v[220:221], v[118:119] op_sel_hi:[1,0]
	v_cvt_pk_bf16_f32 v34, v34, v35
	v_cvt_pk_bf16_f32 v35, v36, v37
	v_pk_mul_f32 v[36:37], v[218:219], v[118:119] op_sel_hi:[1,0]
	global_store_dwordx2 v[48:49], v[34:35], off offset:288
	v_lshlrev_b64 v[34:35], 12, v[120:121]
	s_waitcnt vmcnt(16)
	v_pk_fma_f32 v[32:33], v[36:37], v[32:33], v[96:97]
	v_pk_fma_f32 v[30:31], v[38:39], v[30:31], v[94:95]
	s_nop 0
	v_cvt_pk_bf16_f32 v30, v30, v31
	v_cvt_pk_bf16_f32 v31, v32, v33
	v_lshl_add_u64 v[32:33], s[8:9], 0, v[34:35]
	v_lshl_add_u64 v[32:33], v[32:33], 0, v[134:135]
	global_store_dwordx2 v[32:33], v[30:31], off
	v_pk_mul_f32 v[30:31], v[214:215], v[118:119] op_sel_hi:[1,0]
	v_pk_mul_f32 v[34:35], v[216:217], v[118:119] op_sel_hi:[1,0]
	s_waitcnt vmcnt(16)
	v_pk_fma_f32 v[24:25], v[30:31], v[24:25], v[92:93]
	v_pk_fma_f32 v[22:23], v[34:35], v[22:23], v[90:91]
	s_nop 0
	v_cvt_pk_bf16_f32 v22, v22, v23
	v_cvt_pk_bf16_f32 v23, v24, v25
	v_pk_mul_f32 v[24:25], v[212:213], v[118:119] op_sel_hi:[1,0]
	global_store_dwordx2 v[32:33], v[22:23], off offset:32
	v_pk_mul_f32 v[22:23], v[210:211], v[118:119] op_sel_hi:[1,0]
	s_waitcnt vmcnt(16)
	v_pk_fma_f32 v[24:25], v[24:25], v[26:27], v[86:87]
	v_pk_fma_f32 v[22:23], v[22:23], v[28:29], v[88:89]
	v_cvt_pk_bf16_f32 v24, v24, v25
	s_nop 0
	v_cvt_pk_bf16_f32 v25, v22, v23
	global_store_dwordx2 v[32:33], v[24:25], off offset:256
	v_pk_mul_f32 v[22:23], v[206:207], v[118:119] op_sel_hi:[1,0]
	v_pk_mul_f32 v[24:25], v[208:209], v[118:119] op_sel_hi:[1,0]
	s_waitcnt vmcnt(16)
	v_pk_fma_f32 v[20:21], v[22:23], v[20:21], v[84:85]
	v_pk_fma_f32 v[18:19], v[24:25], v[18:19], v[82:83]
	s_waitcnt vmcnt(15)
	v_pk_mul_f32 v[22:23], v[220:221], v[114:115] op_sel_hi:[1,0]
	v_cvt_pk_bf16_f32 v18, v18, v19
	v_cvt_pk_bf16_f32 v19, v20, v21
	v_pk_mul_f32 v[20:21], v[218:219], v[114:115] op_sel_hi:[1,0]
	global_store_dwordx2 v[32:33], v[18:19], off offset:288
	v_lshlrev_b64 v[18:19], 12, v[116:117]
	s_waitcnt vmcnt(15)
	v_pk_fma_f32 v[12:13], v[20:21], v[12:13], v[80:81]
	v_pk_fma_f32 v[10:11], v[22:23], v[10:11], v[78:79]
	s_nop 0
	v_cvt_pk_bf16_f32 v10, v10, v11
	v_cvt_pk_bf16_f32 v11, v12, v13
	v_lshl_add_u64 v[12:13], s[8:9], 0, v[18:19]
	v_lshl_add_u64 v[12:13], v[12:13], 0, v[134:135]
	global_store_dwordx2 v[12:13], v[10:11], off
	v_pk_mul_f32 v[10:11], v[214:215], v[114:115] op_sel_hi:[1,0]
	v_pk_mul_f32 v[18:19], v[216:217], v[114:115] op_sel_hi:[1,0]
	s_waitcnt vmcnt(15)
	v_pk_fma_f32 v[4:5], v[10:11], v[4:5], v[76:77]
	v_cvt_f32_i32_e32 v11, v15
	v_cvt_f32_i32_e32 v10, v14
	v_cvt_f32_i32_e32 v15, v17
	v_cvt_f32_i32_e32 v14, v16
	v_pk_fma_f32 v[2:3], v[18:19], v[2:3], v[74:75]
	s_nop 0
	v_cvt_pk_bf16_f32 v2, v2, v3
	v_cvt_pk_bf16_f32 v3, v4, v5
	v_pk_mul_f32 v[4:5], v[212:213], v[114:115] op_sel_hi:[1,0]
	global_store_dwordx2 v[12:13], v[2:3], off offset:32
	v_pk_mul_f32 v[2:3], v[210:211], v[114:115] op_sel_hi:[1,0]
	s_waitcnt vmcnt(15)
	v_pk_fma_f32 v[4:5], v[4:5], v[10:11], v[70:71]
	v_pk_fma_f32 v[2:3], v[2:3], v[14:15], v[72:73]
	v_cvt_pk_bf16_f32 v4, v4, v5
	s_nop 0
	v_cvt_pk_bf16_f32 v5, v2, v3
	global_store_dwordx2 v[12:13], v[4:5], off offset:256
	v_pk_mul_f32 v[4:5], v[208:209], v[114:115] op_sel_hi:[1,0]
	v_pk_mul_f32 v[2:3], v[206:207], v[114:115] op_sel_hi:[1,0]
	s_waitcnt vmcnt(15)
	v_pk_fma_f32 v[4:5], v[4:5], v[6:7], v[66:67]
	v_pk_fma_f32 v[2:3], v[2:3], v[8:9], v[68:69]
	v_cvt_pk_bf16_f32 v4, v4, v5
	s_nop 0
	v_cvt_pk_bf16_f32 v5, v2, v3
	global_store_dwordx2 v[12:13], v[4:5], off offset:288
	s_cbranch_vccnz .LBB0_603
	s_andn2_b64 vcc, exec, s[0:1]
	s_cbranch_vccnz .LBB0_602
	s_barrier
	s_branch .LBB0_602
